# speedup vs baseline: 1.0145x; 1.0145x over previous
_Z8k_layer2PKiS0_PKfPKjS2_P15HIP_vector_typeIfLj2EE:
	s_load_dwordx2 s[4:5], s[0:1], 0x18
	s_load_dwordx4 s[8:11], s[0:1], 0x0
	v_lshrrev_b32_e32 v99, 9, v0
	s_nop 0
	v_readfirstlane_b32 s34, v99
	v_or_b32_e32 v72, 0x400, v0
	v_or_b32_e32 v70, 0xc00, v0
	v_or_b32_e32 v1, 0x1400, v0
	v_or_b32_e32 v69, 0x1800, v0
	v_lshlrev_b32_e32 v58, 4, v0
	v_lshlrev_b32_e32 v30, 4, v72
	v_or_b32_e32 v71, 0x800, v0
	v_lshlrev_b32_e32 v34, 4, v70
	v_or_b32_e32 v68, 0x1000, v0
	v_lshlrev_b32_e32 v62, 4, v1
	v_min_u32_e32 v22, 0x1869, v69
	s_waitcnt lgkmcnt(0)
	global_load_dwordx4 v[2:5], v58, s[4:5]
	v_lshlrev_b32_e32 v32, 4, v71
	global_load_dwordx4 v[6:9], v30, s[4:5]
	global_load_dwordx4 v[10:13], v32, s[4:5]
	v_lshlrev_b32_e32 v60, 4, v68
	global_load_dwordx4 v[14:17], v34, s[4:5]
	global_load_dwordx4 v[18:21], v60, s[4:5]
	v_lshlrev_b32_e32 v36, 4, v22
	global_load_dwordx4 v[22:25], v62, s[4:5]
	global_load_dwordx4 v[26:29], v36, s[4:5]
	s_mul_i32 s6, s2, 0x187
	s_ashr_i32 s7, s6, 31
	s_min_i32 s14, s6, 0x18519
	s_lshl_b64 s[2:3], s[6:7], 2
	s_add_u32 s12, s10, s2
	s_addc_u32 s13, s11, s3
	s_ashr_i32 s15, s14, 31
	s_lshl_b64 s[2:3], s[14:15], 2
	s_add_u32 s2, s10, s2
	s_addc_u32 s3, s11, s3
	s_load_dword s16, s[12:13], 0x0
	v_mov_b32_e32 v59, 0
	s_load_dword s2, s[2:3], 0x61c
	v_mov_b32_e32 v31, v59
	v_mov_b32_e32 v33, v59
	v_mov_b32_e32 v35, v59
	v_mov_b32_e32 v61, v59
	s_waitcnt lgkmcnt(0)
	s_sub_i32 s17, s2, s16
	s_add_i32 s7, s17, -1
	v_mov_b32_e32 v63, v59
	v_mov_b32_e32 v37, v59
	s_cmpk_lt_u32 s7, 0x3800
	v_lshl_add_u64 v[94:95], s[4:5], 0, v[58:59]
	v_lshl_add_u64 v[30:31], s[4:5], 0, v[30:31]
	v_lshl_add_u64 v[40:41], s[4:5], 0, v[32:33]
	v_lshl_add_u64 v[38:39], s[4:5], 0, v[34:35]
	v_lshl_add_u64 v[48:49], s[4:5], 0, v[60:61]
	v_lshl_add_u64 v[46:47], s[4:5], 0, v[62:63]
	s_cselect_b64 s[2:3], -1, 0
	s_cmpk_gt_u32 s7, 0x37ff
	v_lshl_add_u64 v[96:97], s[4:5], 0, v[36:37]
	s_cbranch_scc1 .LBB3_2
	v_min_u32_e32 v32, s7, v0
	v_or_b32_e32 v54, 0x1c00, v0
	v_add_u32_e32 v32, s16, v32
	v_min_u32_e32 v34, s7, v72
	v_min_u32_e32 v36, s7, v71
	v_min_u32_e32 v42, s7, v70
	v_min_u32_e32 v44, s7, v68
	v_min_u32_e32 v50, s7, v1
	v_min_u32_e32 v52, s7, v69
	v_min_u32_e32 v54, s7, v54
	v_ashrrev_i32_e32 v33, 31, v32
	v_add_u32_e32 v34, s16, v34
	v_add_u32_e32 v36, s16, v36
	v_add_u32_e32 v42, s16, v42
	v_add_u32_e32 v44, s16, v44
	v_add_u32_e32 v50, s16, v50
	v_add_u32_e32 v52, s16, v52
	v_add_u32_e32 v54, s16, v54
	v_lshl_add_u64 v[32:33], v[32:33], 2, s[8:9]
	v_ashrrev_i32_e32 v35, 31, v34
	v_ashrrev_i32_e32 v37, 31, v36
	v_ashrrev_i32_e32 v43, 31, v42
	v_ashrrev_i32_e32 v45, 31, v44
	v_ashrrev_i32_e32 v51, 31, v50
	v_ashrrev_i32_e32 v53, 31, v52
	v_ashrrev_i32_e32 v55, 31, v54
	v_lshl_add_u64 v[34:35], v[34:35], 2, s[8:9]
	v_lshl_add_u64 v[36:37], v[36:37], 2, s[8:9]
	v_lshl_add_u64 v[42:43], v[42:43], 2, s[8:9]
	v_lshl_add_u64 v[44:45], v[44:45], 2, s[8:9]
	v_lshl_add_u64 v[50:51], v[50:51], 2, s[8:9]
	v_lshl_add_u64 v[52:53], v[52:53], 2, s[8:9]
	v_lshl_add_u64 v[54:55], v[54:55], 2, s[8:9]
	global_load_dword v86, v[32:33], off nt
	global_load_dword v84, v[34:35], off nt
	global_load_dword v83, v[36:37], off nt
	global_load_dword v82, v[42:43], off nt
	global_load_dword v81, v[44:45], off nt
	global_load_dword v79, v[50:51], off nt
	global_load_dword v77, v[52:53], off nt
	global_load_dword v75, v[54:55], off nt
	v_or_b32_e32 v32, 0x2000, v0
	v_min_u32_e32 v32, s7, v32
	v_or_b32_e32 v34, 0x2400, v0
	v_or_b32_e32 v36, 0x2800, v0
	v_or_b32_e32 v42, 0x2c00, v0
	v_or_b32_e32 v44, 0x3000, v0
	v_or_b32_e32 v50, 0x3400, v0
	v_add_u32_e32 v32, s16, v32
	v_min_u32_e32 v34, s7, v34
	v_min_u32_e32 v36, s7, v36
	v_min_u32_e32 v42, s7, v42
	v_min_u32_e32 v44, s7, v44
	v_min_u32_e32 v50, s7, v50
	v_ashrrev_i32_e32 v33, 31, v32
	v_add_u32_e32 v34, s16, v34
	v_add_u32_e32 v36, s16, v36
	v_add_u32_e32 v42, s16, v42
	v_add_u32_e32 v44, s16, v44
	v_add_u32_e32 v50, s16, v50
	v_lshl_add_u64 v[32:33], v[32:33], 2, s[8:9]
	v_ashrrev_i32_e32 v35, 31, v34
	v_ashrrev_i32_e32 v37, 31, v36
	v_ashrrev_i32_e32 v43, 31, v42
	v_ashrrev_i32_e32 v45, 31, v44
	v_ashrrev_i32_e32 v51, 31, v50
	v_lshl_add_u64 v[34:35], v[34:35], 2, s[8:9]
	v_lshl_add_u64 v[36:37], v[36:37], 2, s[8:9]
	v_lshl_add_u64 v[42:43], v[42:43], 2, s[8:9]
	v_lshl_add_u64 v[44:45], v[44:45], 2, s[8:9]
	v_lshl_add_u64 v[50:51], v[50:51], 2, s[8:9]
	global_load_dword v80, v[32:33], off nt
	global_load_dword v78, v[34:35], off nt
	global_load_dword v76, v[36:37], off nt
	global_load_dword v74, v[42:43], off nt
	global_load_dword v73, v[44:45], off nt
	global_load_dword v63, v[50:51], off nt
.LBB3_2:
	s_mov_b32 s7, 0x18000
	v_add_co_u32_e32 v32, vcc, s7, v94
	v_lshrrev_b32_e32 v87, 1, v0
	s_nop 0
	v_addc_co_u32_e32 v33, vcc, 0, v95, vcc
	v_add_co_u32_e32 v34, vcc, s7, v30
	v_add_u32_e32 v64, s6, v87
	s_nop 0
	v_addc_co_u32_e32 v35, vcc, 0, v31, vcc
	v_add_co_u32_e32 v40, vcc, s7, v40
	v_addc_co_u32_e32 v41, vcc, 0, v41, vcc
	v_add_co_u32_e32 v42, vcc, s7, v38
	v_and_b32_e32 v61, 1, v0
	s_nop 0
	v_addc_co_u32_e32 v43, vcc, 0, v39, vcc
	v_add_co_u32_e32 v48, vcc, s7, v48
	v_addc_co_u32_e32 v49, vcc, 0, v49, vcc
	v_add_co_u32_e32 v50, vcc, s7, v46
	s_add_i32 s7, s14, 0x187
	s_nop 0
	v_addc_co_u32_e32 v51, vcc, 0, v47, vcc
	v_add_co_u32_e32 v54, vcc, 0x18000, v96
	v_addc_co_u32_e32 v55, vcc, 0, v97, vcc
	v_cmp_gt_i32_e64 s[6:7], s7, v64
	v_mov_b32_e32 v85, 0
	v_ashrrev_i32_e32 v65, 31, v64
	v_mov_b32_e32 v66, 0
	v_mov_b32_e32 v67, 0
	s_and_saveexec_b64 s[10:11], s[6:7]
	s_cbranch_execz .LBB3_6
	s_load_dwordx2 s[14:15], s[0:1], 0x10
	v_lshlrev_b32_e32 v59, 2, v87
	global_load_dwordx2 v[66:67], v59, s[12:13]
	v_mov_b32_e32 v85, 0
	v_cmp_eq_u32_e32 vcc, 0, v61
	s_waitcnt lgkmcnt(0)
	v_lshl_add_u64 v[88:89], v[64:65], 2, s[14:15]
	global_load_dword v59, v[88:89], off
	s_and_saveexec_b64 s[12:13], vcc
	s_cbranch_execz .LBB3_5
	v_lshl_add_u64 v[88:89], v[64:65], 2, s[4:5]
	global_load_dword v85, v[88:89], off

.LBB3_6:
	s_or_b64 exec, exec, s[10:11]
	global_load_dwordx4 v[30:33], v[32:33], off offset:1696
	s_nop 0
	global_load_dwordx4 v[34:37], v[34:35], off offset:1696
	s_nop 0
	global_load_dwordx4 v[38:41], v[40:41], off offset:1696
	s_nop 0
	global_load_dwordx4 v[42:45], v[42:43], off offset:1696
	s_nop 0
	global_load_dwordx4 v[46:49], v[48:49], off offset:1696
	s_nop 0
	global_load_dwordx4 v[50:53], v[50:51], off offset:1696
	s_nop 0
	global_load_dwordx4 v[54:57], v[54:55], off offset:1696
	s_load_dwordx4 s[12:15], s[0:1], 0x20
	s_andn2_b64 vcc, exec, s[2:3]
	s_cbranch_vccnz .LBB3_30
	v_cmp_gt_u32_e32 vcc, s17, v0
	s_and_saveexec_b64 s[0:1], vcc
	s_cbranch_execnz .LBB3_84
	s_or_b64 exec, exec, s[0:1]
	v_cmp_gt_u32_e32 vcc, s17, v72
	s_and_saveexec_b64 s[0:1], vcc
	s_cbranch_execnz .LBB3_85

.LBB3_30:
	s_waitcnt vmcnt(7)
	s_waitcnt lgkmcnt(0)
	s_load_dwordx2 s[32:33], s[12:13], 0x80
	v_subrev_u32_e32 v63, s16, v61
	s_cmpk_gt_i32 s17, 0x3800
	s_waitcnt vmcnt(7)
	v_add_u32_e32 v63, v63, v66
	v_add_u32_e32 v68, v66, v61
	v_subrev_u32_e32 v66, s16, v67
	s_mov_b64 s[16:17], 0x34d40
	v_lshl_add_u64 v[72:73], v[94:95], 0, s[16:17]
	s_mov_b64 s[16:17], 0x38d40
	v_lshl_add_u64 v[74:75], v[94:95], 0, s[16:17]
	s_mov_b64 s[16:17], 0x3cd40
	v_lshl_add_u64 v[76:77], v[94:95], 0, s[16:17]
	s_mov_b64 s[16:17], 0x40d40
	v_lshl_add_u64 v[78:79], v[94:95], 0, s[16:17]
	s_mov_b64 s[16:17], 0x44d40
	v_lshl_add_u64 v[80:81], v[94:95], 0, s[16:17]
	s_mov_b64 s[16:17], 0x4d3e0
	v_lshl_add_u64 v[86:87], v[94:95], 0, s[16:17]
	s_mov_b64 s[16:17], 0x513e0
	s_waitcnt vmcnt(7)
	v_cvt_f32_f16_sdwa v1, v85 dst_sel:DWORD dst_unused:UNUSED_PAD src0_sel:WORD_1
	v_cvt_f32_f16_e32 v0, v85
	s_movk_i32 s0, 0x186a
	v_lshl_add_u64 v[88:89], v[94:95], 0, s[16:17]
	s_mov_b64 s[16:17], 0x553e0
	v_cmp_gt_u32_e64 s[4:5], s0, v69
	s_mov_b64 s[0:1], 0x30d40
	v_lshl_add_u64 v[90:91], v[94:95], 0, s[16:17]
	s_mov_b64 s[16:17], 0x593e0
	v_lshlrev_b32_e32 v104, 4, v69
	v_lshl_add_u64 v[70:71], v[94:95], 0, s[0:1]
	v_lshl_add_u64 v[82:83], v[96:97], 0, s[0:1]
	s_mov_b64 s[0:1], 0x493e0
	v_lshl_add_u64 v[92:93], v[94:95], 0, s[16:17]
	s_mov_b64 s[16:17], 0x5d3e0
	v_ashrrev_i32_e32 v69, 31, v68
	s_cselect_b64 s[10:11], -1, 0
	v_cmp_lt_i32_e64 s[2:3], v68, v67
	v_lshl_add_u64 v[84:85], v[94:95], 0, s[0:1]
	v_lshl_add_u64 v[94:95], v[94:95], 0, s[16:17]
	v_lshl_add_u64 v[96:97], v[96:97], 0, s[0:1]
	v_lshl_add_u64 v[98:99], v[68:69], 2, s[8:9]
	s_mov_b32 s20, 0
	s_mov_b64 s[8:9], -1
	s_movk_i32 s22, 0x61a8
	v_mov_b32_e32 v69, 0x186a0
	v_mov_b32_e32 v105, 0x186a8
	v_mov_b32_e32 v106, 0x186b0
	v_mov_b32_e32 v107, 0x186b8
	s_branch .LBB3_32
.LBB3_31:
	s_cmp_lg_u64 s[0:1], 0
	s_cbranch_scc1 .Lk4_nopfB2
	s_cmp_eq_u32 s34, 0
	s_cbranch_scc1 .Lk4_nopfB2
	global_load_dwordx4 v[30:33], v[84:85], off
	global_load_dwordx4 v[34:37], v[86:87], off
	global_load_dwordx4 v[38:41], v[88:89], off
	global_load_dwordx4 v[42:45], v[90:91], off
	global_load_dwordx4 v[46:49], v[92:93], off
	global_load_dwordx4 v[50:53], v[94:95], off
	global_load_dwordx4 v[54:57], v[96:97], off

.LBB3_32:
	s_waitcnt vmcnt(13)
	ds_write_b128 v58, v[2:5]
	s_waitcnt vmcnt(12)
	ds_write_b128 v58, v[6:9] offset:16384
	s_waitcnt vmcnt(11)
	ds_write_b128 v58, v[10:13] offset:32768
	s_waitcnt vmcnt(10)
	ds_write_b128 v58, v[14:17] offset:49152
	s_waitcnt vmcnt(9)
	ds_write_b128 v60, v[18:21]
	s_waitcnt vmcnt(8)
	ds_write_b128 v62, v[22:25]
	s_and_saveexec_b64 s[0:1], s[4:5]
	s_cbranch_execz .LBB3_34
	s_waitcnt vmcnt(7)
	ds_write_b128 v104, v[26:29]
.LBB3_34:
	s_or_b64 exec, exec, s[0:1]
	s_mov_b64 s[0:1], -1
	s_and_b64 vcc, exec, s[10:11]
	s_waitcnt lgkmcnt(0)
	s_barrier
	s_cmp_lg_u32 s20, 0
	s_cbranch_scc1 .Lk4_nopfA
	s_cmp_lg_u32 s34, 0
	s_cbranch_scc1 .Lk4_nopfA
	global_load_dwordx4 v[2:5], v[70:71], off
	global_load_dwordx4 v[6:9], v[72:73], off
	global_load_dwordx4 v[10:13], v[74:75], off
	global_load_dwordx4 v[14:17], v[76:77], off
	global_load_dwordx4 v[18:21], v[78:79], off
	global_load_dwordx4 v[22:25], v[80:81], off
	global_load_dwordx4 v[26:29], v[82:83], off
.Lk4_nopfA:
	s_cbranch_vccz .LBB3_42
	v_mov_b64_e32 v[100:101], v[0:1]
	s_and_saveexec_b64 s[0:1], s[2:3]
	s_cbranch_execz .LBB3_41
	s_mov_b64 s[16:17], 0
	v_mov_b64_e32 v[102:103], v[98:99]
	v_mov_b32_e32 v108, v68
	v_mov_b64_e32 v[100:101], v[0:1]
	s_branch .LBB3_38

.LBB3_45:
	v_cmp_lt_i32_e32 vcc, v63, v66
	v_lshl_add_u32 v108, v63, 2, v69
	v_add_u32_e32 v109, 2, v63
	v_add_u32_e32 v110, 4, v63
	v_cndmask_b32_e32 v108, v69, v108, vcc
	v_cmp_lt_i32_e64 s[24:25], v109, v66
	v_add_u32_e32 v111, 6, v63
	ds_read2_b32 v[100:101], v108 offset1:2
	ds_read2_b32 v[102:103], v108 offset0:4 offset1:6
	v_cmp_lt_i32_e64 s[26:27], v110, v66
	v_cmp_lt_i32_e64 s[28:29], v111, v66
	s_waitcnt lgkmcnt(0)
	v_subrev_u32_e32 v100, s20, v100
	v_subrev_u32_e32 v101, s20, v101
	v_subrev_u32_e32 v102, s20, v102
	v_subrev_u32_e32 v103, s20, v103
	v_cndmask_b32_e32 v100, -1, v100, vcc
	v_cndmask_b32_e64 v101, -1, v101, s[24:25]
	v_cndmask_b32_e64 v102, -1, v102, s[26:27]
	v_cndmask_b32_e64 v103, -1, v103, s[28:29]
	v_min_u32_e32 v108, 0x61a7, v100
	v_min_u32_e32 v109, 0x61a7, v101
	v_min_u32_e32 v110, 0x61a7, v102
	v_min_u32_e32 v111, 0x61a7, v103
	v_lshlrev_b32_e32 v108, 2, v108
	v_lshlrev_b32_e32 v109, 2, v109
	v_lshlrev_b32_e32 v110, 2, v110
	v_lshlrev_b32_e32 v111, 2, v111
	ds_read_b32 v108, v108
	ds_read_b32 v109, v109
	ds_read_b32 v110, v110
	ds_read_b32 v111, v111
	v_cmp_gt_u32_e32 vcc, s22, v100
	v_cmp_gt_u32_e64 s[24:25], s22, v101
	v_cmp_gt_u32_e64 s[26:27], s22, v102
	v_cmp_gt_u32_e64 s[28:29], s22, v103
	s_nop 0
	v_cndmask_b32_e64 v112, 0, 1, vcc
	v_addc_co_u32_e64 v112, s[30:31], 0, v112, s[24:25]
	v_addc_co_u32_e64 v112, s[30:31], 0, v112, s[26:27]
	v_addc_co_u32_e64 v112, s[30:31], 0, v112, s[28:29]
	s_waitcnt lgkmcnt(0)
	v_cndmask_b32_e32 v108, 0, v108, vcc
	v_cndmask_b32_e64 v109, 0, v109, s[24:25]
	v_cndmask_b32_e64 v110, 0, v110, s[26:27]
	v_cndmask_b32_e64 v111, 0, v111, s[28:29]
	v_cvt_f32_f16_e32 v100, v108
	v_cvt_f32_f16_sdwa v101, v108 dst_sel:DWORD dst_unused:UNUSED_PAD src0_sel:WORD_1
	v_cvt_f32_f16_e32 v102, v109
	v_cvt_f32_f16_sdwa v103, v109 dst_sel:DWORD dst_unused:UNUSED_PAD src0_sel:WORD_1
	v_cvt_f32_f16_e32 v108, v110
	v_cvt_f32_f16_sdwa v109, v110 dst_sel:DWORD dst_unused:UNUSED_PAD src0_sel:WORD_1
	v_cvt_f32_f16_e32 v110, v111
	v_cvt_f32_f16_sdwa v111, v111 dst_sel:DWORD dst_unused:UNUSED_PAD src0_sel:WORD_1
	v_pk_add_f32 v[0:1], v[0:1], v[100:101]
	v_cmp_gt_u32_e32 vcc, 4, v112
	v_pk_add_f32 v[0:1], v[0:1], v[102:103]
	s_or_b64 s[16:17], vcc, s[16:17]
	v_pk_add_f32 v[0:1], v[0:1], v[108:109]
	v_lshl_add_u32 v63, v112, 1, v63
	v_pk_add_f32 v[0:1], v[0:1], v[110:111]
	s_andn2_b64 exec, exec, s[16:17]
	s_cbranch_execnz .LBB3_45
	s_branch .LBB3_54

.LBB3_55:
	s_cmp_lg_u32 s20, 0
	s_cbranch_scc1 .Lk4_nopfA2
	s_cmp_eq_u32 s34, 0
	s_cbranch_scc1 .Lk4_nopfA2
	global_load_dwordx4 v[2:5], v[70:71], off
	global_load_dwordx4 v[6:9], v[72:73], off
	global_load_dwordx4 v[10:13], v[74:75], off
	global_load_dwordx4 v[14:17], v[76:77], off
	global_load_dwordx4 v[18:21], v[78:79], off
	global_load_dwordx4 v[22:25], v[80:81], off
	global_load_dwordx4 v[26:29], v[82:83], off

.LBB3_57:
	s_barrier
	s_cmp_eq_u32 s20, 0
	s_cbranch_scc1 .Lk4_oddw_first
	s_waitcnt vmcnt(6)
	ds_write_b128 v58, v[30:33]
	s_waitcnt vmcnt(5)
	ds_write_b128 v58, v[34:37] offset:16384
	s_waitcnt vmcnt(4)
	ds_write_b128 v58, v[38:41] offset:32768
	s_waitcnt vmcnt(3)
	ds_write_b128 v58, v[42:45] offset:49152
	s_waitcnt vmcnt(2)
	ds_write_b128 v60, v[46:49]
	s_waitcnt vmcnt(1)
	ds_write_b128 v62, v[50:53]
	s_and_saveexec_b64 s[8:9], s[4:5]
	s_cbranch_execz .LBB3_59
	s_waitcnt vmcnt(0)
	ds_write_b128 v104, v[54:57]
	s_branch .LBB3_59
.Lk4_oddw_first:
	s_waitcnt vmcnt(13)
	ds_write_b128 v58, v[30:33]
	s_waitcnt vmcnt(12)
	ds_write_b128 v58, v[34:37] offset:16384
	s_waitcnt vmcnt(11)
	ds_write_b128 v58, v[38:41] offset:32768
	s_waitcnt vmcnt(10)
	ds_write_b128 v58, v[42:45] offset:49152
	s_waitcnt vmcnt(9)
	ds_write_b128 v60, v[46:49]
	s_waitcnt vmcnt(8)
	ds_write_b128 v62, v[50:53]
	s_and_saveexec_b64 s[8:9], s[4:5]
	s_cbranch_execz .LBB3_59
	s_waitcnt vmcnt(7)
	ds_write_b128 v104, v[54:57]
.LBB3_59:
	s_or_b64 exec, exec, s[8:9]
	s_add_i32 s23, s20, 0x61a8
	s_mov_b64 s[8:9], -1
	s_and_b64 vcc, exec, s[10:11]
	s_waitcnt lgkmcnt(0)
	s_barrier
	s_cmp_lg_u32 s20, 0
	s_cbranch_scc1 .Lk4_nopfB
	s_cmp_lg_u32 s34, 0
	s_cbranch_scc1 .Lk4_nopfB
	global_load_dwordx4 v[30:33], v[84:85], off
	global_load_dwordx4 v[34:37], v[86:87], off
	global_load_dwordx4 v[38:41], v[88:89], off
	global_load_dwordx4 v[42:45], v[90:91], off
	global_load_dwordx4 v[46:49], v[92:93], off
	global_load_dwordx4 v[50:53], v[94:95], off
	global_load_dwordx4 v[54:57], v[96:97], off
.Lk4_nopfB:
	s_cbranch_vccz .LBB3_67
	v_mov_b64_e32 v[100:101], v[0:1]
	s_and_saveexec_b64 s[8:9], s[2:3]
	s_cbranch_execz .LBB3_66
	s_mov_b64 s[18:19], 0
	v_mov_b64_e32 v[102:103], v[98:99]
	v_mov_b32_e32 v108, v68
	v_mov_b64_e32 v[100:101], v[0:1]
	s_branch .LBB3_63

.LBB3_70:
	v_cmp_lt_i32_e32 vcc, v63, v66
	v_lshl_add_u32 v108, v63, 2, v69
	v_add_u32_e32 v109, 2, v63
	v_add_u32_e32 v110, 4, v63
	v_cndmask_b32_e32 v108, v69, v108, vcc
	v_cmp_lt_i32_e64 s[24:25], v109, v66
	v_add_u32_e32 v111, 6, v63
	ds_read2_b32 v[100:101], v108 offset1:2
	ds_read2_b32 v[102:103], v108 offset0:4 offset1:6
	v_cmp_lt_i32_e64 s[26:27], v110, v66
	v_cmp_lt_i32_e64 s[28:29], v111, v66
	s_waitcnt lgkmcnt(0)
	v_subrev_u32_e32 v100, s23, v100
	v_subrev_u32_e32 v101, s23, v101
	v_subrev_u32_e32 v102, s23, v102
	v_subrev_u32_e32 v103, s23, v103
	v_cndmask_b32_e32 v100, -1, v100, vcc
	v_cndmask_b32_e64 v101, -1, v101, s[24:25]
	v_cndmask_b32_e64 v102, -1, v102, s[26:27]
	v_cndmask_b32_e64 v103, -1, v103, s[28:29]
	v_min_u32_e32 v108, 0x61a7, v100
	v_min_u32_e32 v109, 0x61a7, v101
	v_min_u32_e32 v110, 0x61a7, v102
	v_min_u32_e32 v111, 0x61a7, v103
	v_lshlrev_b32_e32 v108, 2, v108
	v_lshlrev_b32_e32 v109, 2, v109
	v_lshlrev_b32_e32 v110, 2, v110
	v_lshlrev_b32_e32 v111, 2, v111
	ds_read_b32 v108, v108
	ds_read_b32 v109, v109
	ds_read_b32 v110, v110
	ds_read_b32 v111, v111
	v_cmp_gt_u32_e32 vcc, s22, v100
	v_cmp_gt_u32_e64 s[24:25], s22, v101
	v_cmp_gt_u32_e64 s[26:27], s22, v102
	v_cmp_gt_u32_e64 s[28:29], s22, v103
	s_nop 0
	v_cndmask_b32_e64 v112, 0, 1, vcc
	v_addc_co_u32_e64 v112, s[30:31], 0, v112, s[24:25]
	v_addc_co_u32_e64 v112, s[30:31], 0, v112, s[26:27]
	v_addc_co_u32_e64 v112, s[30:31], 0, v112, s[28:29]
	s_waitcnt lgkmcnt(0)
	v_cndmask_b32_e32 v108, 0, v108, vcc
	v_cndmask_b32_e64 v109, 0, v109, s[24:25]
	v_cndmask_b32_e64 v110, 0, v110, s[26:27]
	v_cndmask_b32_e64 v111, 0, v111, s[28:29]
	v_cvt_f32_f16_e32 v100, v108
	v_cvt_f32_f16_sdwa v101, v108 dst_sel:DWORD dst_unused:UNUSED_PAD src0_sel:WORD_1
	v_cvt_f32_f16_e32 v102, v109
	v_cvt_f32_f16_sdwa v103, v109 dst_sel:DWORD dst_unused:UNUSED_PAD src0_sel:WORD_1
	v_cvt_f32_f16_e32 v108, v110
	v_cvt_f32_f16_sdwa v109, v110 dst_sel:DWORD dst_unused:UNUSED_PAD src0_sel:WORD_1
	v_cvt_f32_f16_e32 v110, v111
	v_cvt_f32_f16_sdwa v111, v111 dst_sel:DWORD dst_unused:UNUSED_PAD src0_sel:WORD_1
	v_pk_add_f32 v[0:1], v[0:1], v[100:101]
	v_cmp_gt_u32_e32 vcc, 4, v112
	v_pk_add_f32 v[0:1], v[0:1], v[102:103]
	s_or_b64 s[18:19], vcc, s[18:19]
	v_pk_add_f32 v[0:1], v[0:1], v[108:109]
	v_lshl_add_u32 v63, v112, 1, v63
	v_pk_add_f32 v[0:1], v[0:1], v[110:111]
	s_andn2_b64 exec, exec, s[18:19]
	s_cbranch_execnz .LBB3_70
	s_branch .LBB3_79

.LBB3_80:
	s_branch .LBB3_31
.LBB3_81:
	s_waitcnt vmcnt(6)
	v_mbcnt_lo_u32_b32 v2, -1, 0
	v_mbcnt_hi_u32_b32 v2, -1, v2
	v_and_b32_e32 v4, 64, v2
	v_xor_b32_e32 v3, 1, v2
	v_add_u32_e32 v4, 64, v4
	v_cmp_lt_i32_e32 vcc, v3, v4
	s_nop 1
	v_cndmask_b32_e32 v2, v2, v3, vcc
	v_lshlrev_b32_e32 v3, 2, v2
	ds_bpermute_b32 v2, v3, v0
	ds_bpermute_b32 v3, v3, v1
	v_cmp_eq_u32_e32 vcc, 0, v61
	s_and_b64 s[0:1], vcc, s[6:7]
	s_and_saveexec_b64 s[2:3], s[0:1]
	s_cbranch_execz .LBB3_83
	s_waitcnt lgkmcnt(0)
	v_pk_add_f32 v[0:1], v[0:1], v[2:3]
	v_mov_b32_e32 v2, v59
	v_lshl_add_u64 v[4:5], v[64:65], 3, s[14:15]
	v_pk_fma_f32 v[0:1], v[2:3], v[0:1], s[32:33] op_sel_hi:[0,1,1]
	global_store_dwordx2 v[4:5], v[0:1], off

	.amdhsa_kernel _Z8k_layer2PKiS0_PKfPKjS2_P15HIP_vector_typeIfLj2EE
		.amdhsa_group_segment_fixed_size 157408
		.amdhsa_private_segment_fixed_size 0
		.amdhsa_kernarg_size 48
		.amdhsa_user_sgpr_count 2
		.amdhsa_user_sgpr_dispatch_ptr 0
		.amdhsa_user_sgpr_queue_ptr 0
		.amdhsa_user_sgpr_kernarg_segment_ptr 1
		.amdhsa_user_sgpr_dispatch_id 0
		.amdhsa_user_sgpr_kernarg_preload_length 0
		.amdhsa_user_sgpr_kernarg_preload_offset 0
		.amdhsa_user_sgpr_private_segment_size 0
		.amdhsa_uses_dynamic_stack 0
		.amdhsa_enable_private_segment 0
		.amdhsa_system_sgpr_workgroup_id_x 1
		.amdhsa_system_sgpr_workgroup_id_y 0
		.amdhsa_system_sgpr_workgroup_id_z 0
		.amdhsa_system_sgpr_workgroup_info 0
		.amdhsa_system_vgpr_workitem_id 0
		.amdhsa_next_free_vgpr 114
		.amdhsa_next_free_sgpr 96
		.amdhsa_accum_offset 116
		.amdhsa_reserve_vcc 1
		.amdhsa_float_round_mode_32 0
		.amdhsa_float_round_mode_16_64 0
		.amdhsa_float_denorm_mode_32 3
		.amdhsa_float_denorm_mode_16_64 3
		.amdhsa_dx10_clamp 1
		.amdhsa_ieee_mode 1
		.amdhsa_fp16_overflow 0
		.amdhsa_tg_split 0
		.amdhsa_exception_fp_ieee_invalid_op 0
		.amdhsa_exception_fp_denorm_src 0
		.amdhsa_exception_fp_ieee_div_zero 0
		.amdhsa_exception_fp_ieee_overflow 0
		.amdhsa_exception_fp_ieee_underflow 0
		.amdhsa_exception_fp_ieee_inexact 0
		.amdhsa_exception_int_div_zero 0
	.end_amdhsa_kernel

amdhsa.kernels:
  - .agpr_count:     0
    .args:
      - .actual_access:  read_only
        .address_space:  global
        .offset:         0
        .size:           8
        .value_kind:     global_buffer
      - .actual_access:  read_only
        .address_space:  global
        .offset:         8
        .size:           8
        .value_kind:     global_buffer
      - .actual_access:  write_only
        .address_space:  global
        .offset:         16
        .size:           8
        .value_kind:     global_buffer
      - .actual_access:  write_only
        .address_space:  global
        .offset:         24
        .size:           8
        .value_kind:     global_buffer
      - .actual_access:  read_only
        .address_space:  global
        .offset:         32
        .size:           8
        .value_kind:     global_buffer
      - .actual_access:  read_only
        .address_space:  global
        .offset:         40
        .size:           8
        .value_kind:     global_buffer
      - .actual_access:  read_only
        .address_space:  global
        .offset:         48
        .size:           8
        .value_kind:     global_buffer
      - .actual_access:  read_only
        .address_space:  global
        .offset:         56
        .size:           8
        .value_kind:     global_buffer
      - .actual_access:  write_only
        .address_space:  global
        .offset:         64
        .size:           8
        .value_kind:     global_buffer
      - .actual_access:  read_only
        .address_space:  global
        .offset:         72
        .size:           8
        .value_kind:     global_buffer
      - .actual_access:  write_only
        .address_space:  global
        .offset:         80
        .size:           8
        .value_kind:     global_buffer
    .group_segment_fixed_size: 55632
    .kernarg_segment_align: 8
    .kernarg_segment_size: 88
    .language:       OpenCL C
    .language_version:
      - 2
      - 0
    .max_flat_workgroup_size: 1024
    .name:           _Z9k_scatterPKiS0_PiPjPKfS4_S4_S4_PfS4_PDv4_j
    .private_segment_fixed_size: 0
    .sgpr_count:     58
    .sgpr_spill_count: 0
    .symbol:         _Z9k_scatterPKiS0_PiPjPKfS4_S4_S4_PfS4_PDv4_j.kd
    .uniform_work_group_size: 1
    .uses_dynamic_stack: false
    .vgpr_count:     114
    .vgpr_spill_count: 0
    .wavefront_size: 64
  - .agpr_count:     0
    .args:
      - .actual_access:  read_only
        .address_space:  global
        .offset:         0
        .size:           8
        .value_kind:     global_buffer
      - .actual_access:  read_only
        .address_space:  global
        .offset:         8
        .size:           8
        .value_kind:     global_buffer
      - .actual_access:  read_only
        .address_space:  global
        .offset:         16
        .size:           8
        .value_kind:     global_buffer
      - .actual_access:  read_only
        .address_space:  global
        .offset:         24
        .size:           8
        .value_kind:     global_buffer
      - .actual_access:  write_only
        .address_space:  global
        .offset:         32
        .size:           8
        .value_kind:     global_buffer
      - .actual_access:  write_only
        .address_space:  global
        .offset:         40
        .size:           8
        .value_kind:     global_buffer
      - .actual_access:  write_only
        .address_space:  global
        .offset:         48
        .size:           8
        .value_kind:     global_buffer
      - .actual_access:  write_only
        .address_space:  global
        .offset:         56
        .size:           8
        .value_kind:     global_buffer
    .group_segment_fixed_size: 37232
    .kernarg_segment_align: 8
    .kernarg_segment_size: 64
    .language:       OpenCL C
    .language_version:
      - 2
      - 0
    .max_flat_workgroup_size: 256
    .name:           _Z9k_binsortPKjPKiPKfPKDv4_jPiS8_PfP6__half
    .private_segment_fixed_size: 0
    .sgpr_count:     104
    .sgpr_spill_count: 0
    .symbol:         _Z9k_binsortPKjPKiPKfPKDv4_jPiS8_PfP6__half.kd
    .uniform_work_group_size: 1
    .uses_dynamic_stack: false
    .vgpr_count:     168
    .vgpr_spill_count: 0
    .wavefront_size: 64
  - .agpr_count:     0
    .args:
      - .actual_access:  read_only
        .address_space:  global
        .offset:         0
        .size:           8
        .value_kind:     global_buffer
      - .actual_access:  read_only
        .address_space:  global
        .offset:         8
        .size:           8
        .value_kind:     global_buffer
      - .actual_access:  read_only
        .address_space:  global
        .offset:         16
        .size:           8
        .value_kind:     global_buffer
      - .actual_access:  read_only
        .address_space:  global
        .offset:         24
        .size:           8
        .value_kind:     global_buffer
      - .actual_access:  read_only
        .address_space:  global
        .offset:         32
        .size:           8
        .value_kind:     global_buffer
      - .actual_access:  read_only
        .address_space:  global
        .offset:         40
        .size:           8
        .value_kind:     global_buffer
      - .actual_access:  write_only
        .address_space:  global
        .offset:         48
        .size:           8
        .value_kind:     global_buffer
    .group_segment_fixed_size: 6272
    .kernarg_segment_align: 8
    .kernarg_segment_size: 56
    .language:       OpenCL C
    .language_version:
      - 2
      - 0
    .max_flat_workgroup_size: 64
    .name:           _Z8k_layer1PKiS0_PKfPK6__halfS2_S2_P7__half2
    .private_segment_fixed_size: 0
    .sgpr_count:     22
    .sgpr_spill_count: 0
    .symbol:         _Z8k_layer1PKiS0_PKfPK6__halfS2_S2_P7__half2.kd
    .uniform_work_group_size: 1
    .uses_dynamic_stack: false
    .vgpr_count:     70
    .vgpr_spill_count: 0
    .wavefront_size: 64
  - .agpr_count:     0
    .args:
      - .actual_access:  read_only
        .address_space:  global
        .offset:         0
        .size:           8
        .value_kind:     global_buffer
      - .actual_access:  read_only
        .address_space:  global
        .offset:         8
        .size:           8
        .value_kind:     global_buffer
      - .actual_access:  read_only
        .address_space:  global
        .offset:         16
        .size:           8
        .value_kind:     global_buffer
      - .actual_access:  read_only
        .address_space:  global
        .offset:         24
        .size:           8
        .value_kind:     global_buffer
      - .actual_access:  read_only
        .address_space:  global
        .offset:         32
        .size:           8
        .value_kind:     global_buffer
      - .actual_access:  write_only
        .address_space:  global
        .offset:         40
        .size:           8
        .value_kind:     global_buffer
    .group_segment_fixed_size: 157408
    .kernarg_segment_align: 8
    .kernarg_segment_size: 48
    .language:       OpenCL C
    .language_version:
      - 2
      - 0
    .max_flat_workgroup_size: 1024
    .name:           _Z8k_layer2PKiS0_PKfPKjS2_P15HIP_vector_typeIfLj2EE
    .private_segment_fixed_size: 0
    .sgpr_count:     30
    .sgpr_spill_count: 0
    .symbol:         _Z8k_layer2PKiS0_PKfPKjS2_P15HIP_vector_typeIfLj2EE.kd
    .uniform_work_group_size: 1
    .uses_dynamic_stack: false
    .vgpr_count:     114
    .vgpr_spill_count: 0
    .wavefront_size: 64
  - .agpr_count:     0
    .args:
      - .actual_access:  read_only
        .address_space:  global
        .offset:         0
        .size:           8
        .value_kind:     global_buffer
      - .actual_access:  read_only
        .address_space:  global
        .offset:         8
        .size:           8
        .value_kind:     global_buffer
      - .actual_access:  write_only
        .address_space:  global
        .offset:         16
        .size:           8
        .value_kind:     global_buffer
    .group_segment_fixed_size: 0
    .kernarg_segment_align: 8
    .kernarg_segment_size: 24
    .language:       OpenCL C
    .language_version:
      - 2
      - 0
    .max_flat_workgroup_size: 256
    .name:           _Z5k_outPK15HIP_vector_typeIiLj4EEPKS_IfLj2EEPS3_
    .private_segment_fixed_size: 0
    .sgpr_count:     14
    .sgpr_spill_count: 0
    .symbol:         _Z5k_outPK15HIP_vector_typeIiLj4EEPKS_IfLj2EEPS3_.kd
    .uniform_work_group_size: 1
    .uses_dynamic_stack: false
    .vgpr_count:     14
    .vgpr_spill_count: 0
    .wavefront_size: 64
